# P8 epilogue Y2 scatter stores back to plain write-back (the 64-byte row pieces merge in L2)
# speedup vs baseline: 1.0008x; 1.0008x over previous
; __device__ __forceinline__ unsigned cvt_pk_bf16(float lo, float hi) { unsigned r; asm volatile("v_cvt_pk_bf16_f32 %0, %1, %2" : "=v"(r) : "v"(lo), "v"(hi)); return r; }
;     template <class Tp> __device__ __forceinline__ Tp* w(size_t off) const { return (Tp*)(ws + off); }
;     __device__ __forceinline__ void operator()(const f32x4 (&acc)[2][2][4][2], const Unit& u, int wr, int wc, int fr, int fq) const {
;         const int e = u.pn >> 3, lim = offs[e] + cnts[e], lb = e * 16384 - offs[e];
;         const int row0 = u.pm * BM + wr * 64 + fr, col0 = (u.pn & 7) * BM + wc * 32 + 8 * fq;
; #pragma unroll
;         for (int ai = 0; ai < 2; ++ai)
; #pragma unroll
;             for (int m = 0; m < 4; ++m) { const int p = row0 + ai * HALF + m * 16;
;                 if (p < lim) { const float w = wrow[lb + p]; bf16_t* rowp = Y2 + (size_t)tsi[lb + p] * 2048 + col0;
; #pragma unroll
;                     for (int bj = 0; bj < 2; ++bj) { const f32x4 v0 = acc[ai][bj][m][0] * w, v1 = acc[ai][bj][m][1] * w;
;                         u32x4 o; o.x = cvt_pk_bf16(v0[0], v0[1]); o.y = cvt_pk_bf16(v0[2], v0[3]); o.z = cvt_pk_bf16(v1[0], v1[1]); o.w = cvt_pk_bf16(v1[2], v1[3]);
;                         *(u32x4*)(rowp + bj * HALF) = o; } } }
;     }
.LBB0_1326:
	s_ashr_i32 s10, s56, 3
	s_lshl_b32 s11, s10, 2
	s_add_i32 s11, s11, 0
	s_add_i32 s12, s11, 0x20000
	s_add_i32 s11, s11, 0x20200
	v_mov_b32_e32 v2, s12
	v_mov_b32_e32 v3, s11
	ds_read_b32 v2, v2
	ds_read_b32 v3, v3
	s_lshl_b32 s10, s10, 14
	v_lshl_add_u32 v203, s55, 8, v219
	s_waitcnt lgkmcnt(0)
	v_sub_u32_e32 v199, s10, v2
	s_lshl_b32 s10, s56, 8
	s_and_b32 s10, s10, 0x700
	v_add_u32_e32 v201, v3, v2
	v_or_b32_e32 v2, s10, v224
	v_add_u32_e32 v208, 0, v203
	v_cmp_lt_i32_e32 vcc, v208, v201
	s_and_saveexec_b64 s[10:11], vcc
	v_add_u32_e32 v208, v199, v208
	v_ashrrev_i32_e32 v209, 31, v208
	v_lshlrev_b64 v[208:209], 2, v[208:209]
	v_lshl_add_u64 v[210:211], s[30:31], 0, v[208:209]
	v_lshl_add_u64 v[208:209], s[28:29], 0, v[208:209]
	global_load_dword v116, v[208:209], off
	global_load_dword v132, v[210:211], off
	s_or_b64 exec, exec, s[10:11]
	v_add_u32_e32 v208, 16, v203
	v_cmp_lt_i32_e32 vcc, v208, v201
	s_and_saveexec_b64 s[10:11], vcc
	v_add_u32_e32 v208, v199, v208
	v_ashrrev_i32_e32 v209, 31, v208
	v_lshlrev_b64 v[208:209], 2, v[208:209]
	v_lshl_add_u64 v[210:211], s[30:31], 0, v[208:209]
	v_lshl_add_u64 v[208:209], s[28:29], 0, v[208:209]
	global_load_dword v117, v[208:209], off
	global_load_dword v133, v[210:211], off
	s_or_b64 exec, exec, s[10:11]
	v_add_u32_e32 v208, 32, v203
	v_cmp_lt_i32_e32 vcc, v208, v201
	s_and_saveexec_b64 s[10:11], vcc
	v_add_u32_e32 v208, v199, v208
	v_ashrrev_i32_e32 v209, 31, v208
	v_lshlrev_b64 v[208:209], 2, v[208:209]
	v_lshl_add_u64 v[210:211], s[30:31], 0, v[208:209]
	v_lshl_add_u64 v[208:209], s[28:29], 0, v[208:209]
	global_load_dword v118, v[208:209], off
	global_load_dword v134, v[210:211], off
	s_or_b64 exec, exec, s[10:11]
	v_add_u32_e32 v208, 48, v203
	v_cmp_lt_i32_e32 vcc, v208, v201
	s_and_saveexec_b64 s[10:11], vcc
	v_add_u32_e32 v208, v199, v208
	v_ashrrev_i32_e32 v209, 31, v208
	v_lshlrev_b64 v[208:209], 2, v[208:209]
	v_lshl_add_u64 v[210:211], s[30:31], 0, v[208:209]
	v_lshl_add_u64 v[208:209], s[28:29], 0, v[208:209]
	global_load_dword v119, v[208:209], off
	global_load_dword v135, v[210:211], off
	s_or_b64 exec, exec, s[10:11]
	v_add_u32_e32 v208, 0x80, v203
	v_cmp_lt_i32_e32 vcc, v208, v201
	s_and_saveexec_b64 s[10:11], vcc
	v_add_u32_e32 v208, v199, v208
	v_ashrrev_i32_e32 v209, 31, v208
	v_lshlrev_b64 v[208:209], 2, v[208:209]
	v_lshl_add_u64 v[210:211], s[30:31], 0, v[208:209]
	v_lshl_add_u64 v[208:209], s[28:29], 0, v[208:209]
	global_load_dword v124, v[208:209], off
	global_load_dword v140, v[210:211], off
	s_or_b64 exec, exec, s[10:11]
	v_add_u32_e32 v208, 0x90, v203
	v_cmp_lt_i32_e32 vcc, v208, v201
	s_and_saveexec_b64 s[10:11], vcc
	v_add_u32_e32 v208, v199, v208
	v_ashrrev_i32_e32 v209, 31, v208
	v_lshlrev_b64 v[208:209], 2, v[208:209]
	v_lshl_add_u64 v[210:211], s[30:31], 0, v[208:209]
	v_lshl_add_u64 v[208:209], s[28:29], 0, v[208:209]
	global_load_dword v125, v[208:209], off
	global_load_dword v141, v[210:211], off
	s_or_b64 exec, exec, s[10:11]
	v_add_u32_e32 v208, 0xa0, v203
	v_cmp_lt_i32_e32 vcc, v208, v201
	s_and_saveexec_b64 s[10:11], vcc
	v_add_u32_e32 v208, v199, v208
	v_ashrrev_i32_e32 v209, 31, v208
	v_lshlrev_b64 v[208:209], 2, v[208:209]
	v_lshl_add_u64 v[210:211], s[30:31], 0, v[208:209]
	v_lshl_add_u64 v[208:209], s[28:29], 0, v[208:209]
	global_load_dword v126, v[208:209], off
	global_load_dword v142, v[210:211], off
	s_or_b64 exec, exec, s[10:11]
	v_add_u32_e32 v208, 0xb0, v203
	v_cmp_lt_i32_e32 vcc, v208, v201
	s_and_saveexec_b64 s[10:11], vcc
	v_add_u32_e32 v208, v199, v208
	v_ashrrev_i32_e32 v209, 31, v208
	v_lshlrev_b64 v[208:209], 2, v[208:209]
	v_lshl_add_u64 v[210:211], s[30:31], 0, v[208:209]
	v_lshl_add_u64 v[208:209], s[28:29], 0, v[208:209]
	global_load_dword v127, v[208:209], off
	global_load_dword v143, v[210:211], off
	s_or_b64 exec, exec, s[10:11]
	s_waitcnt vmcnt(0)
	v_cmp_lt_i32_e32 vcc, v203, v201
	v_lshlrev_b32_e32 v2, 1, v2
	s_and_saveexec_b64 s[10:11], vcc
	s_cbranch_execz .LBB0_1328
	v_mov_b32_e32 v208, v116
	v_mov_b32_e32 v210, v132
	v_mov_b32_e32 v3, v1
	v_ashrrev_i32_e32 v209, 31, v208
	v_pk_mul_f32 v[212:213], v[186:187], v[210:211] op_sel_hi:[1,0]
	v_lshlrev_b64 v[240:241], 12, v[208:209]
	v_pk_mul_f32 v[226:227], v[184:185], v[210:211] op_sel_hi:[1,0]
	v_pk_mul_f32 v[228:229], v[178:179], v[210:211] op_sel_hi:[1,0]
	v_cvt_pk_bf16_f32 v208, v226, v227
	v_cvt_pk_bf16_f32 v209, v212, v213
	v_lshl_add_u64 v[212:213], s[26:27], 0, v[240:241]
	v_pk_mul_f32 v[230:231], v[176:177], v[210:211] op_sel_hi:[1,0]
	v_pk_mul_f32 v[232:233], v[146:147], v[210:211] op_sel_hi:[1,0]
	v_pk_mul_f32 v[234:235], v[144:145], v[210:211] op_sel_hi:[1,0]
	v_pk_mul_f32 v[236:237], v[138:139], v[210:211] op_sel_hi:[1,0]
	v_pk_mul_f32 v[238:239], v[136:137], v[210:211] op_sel_hi:[1,0]
	v_cvt_pk_bf16_f32 v210, v230, v231
	v_cvt_pk_bf16_f32 v211, v228, v229
	v_lshl_add_u64 v[212:213], v[212:213], 0, v[2:3]
	global_store_dwordx4 v[212:213], v[208:211], off
	s_nop 1
	v_cvt_pk_bf16_f32 v208, v234, v235
	v_cvt_pk_bf16_f32 v209, v232, v233
	v_cvt_pk_bf16_f32 v210, v238, v239
	v_cvt_pk_bf16_f32 v211, v236, v237
	global_store_dwordx4 v[212:213], v[208:211], off offset:256
; __device__ __forceinline__ unsigned cvt_pk_bf16(float lo, float hi) { unsigned r; asm volatile("v_cvt_pk_bf16_f32 %0, %1, %2" : "=v"(r) : "v"(lo), "v"(hi)); return r; }
;     template <class Tp> __device__ __forceinline__ Tp* w(size_t off) const { return (Tp*)(ws + off); }
;     __device__ __forceinline__ void operator()(const f32x4 (&acc)[2][2][4][2], const Unit& u, int wr, int wc, int fr, int fq) const {
;     ...
;             for (int m = 0; m < 4; ++m) { const int p = row0 + ai * HALF + m * 16;
;                 if (p < lim) { const float w = wrow[lb + p]; bf16_t* rowp = Y2 + (size_t)tsi[lb + p] * 2048 + col0;
; #pragma unroll
;                     for (int bj = 0; bj < 2; ++bj) { const f32x4 v0 = acc[ai][bj][m][0] * w, v1 = acc[ai][bj][m][1] * w;
;                         u32x4 o; o.x = cvt_pk_bf16(v0[0], v0[1]); o.y = cvt_pk_bf16(v0[2], v0[3]); o.z = cvt_pk_bf16(v1[0], v1[1]); o.w = cvt_pk_bf16(v1[2], v1[3]);
;                         *(u32x4*)(rowp + bj * HALF) = o; } } }
.LBB0_1328:
	s_or_b64 exec, exec, s[10:11]
	v_or_b32_e32 v3, 16, v203
	v_cmp_lt_i32_e32 vcc, v3, v201
	s_and_saveexec_b64 s[10:11], vcc
	s_cbranch_execz .LBB0_1330
	v_mov_b32_e32 v208, v117
	v_mov_b32_e32 v210, v133
	v_mov_b32_e32 v3, v1
	v_ashrrev_i32_e32 v209, 31, v208
	v_pk_mul_f32 v[212:213], v[170:171], v[210:211] op_sel_hi:[1,0]
	v_lshlrev_b64 v[240:241], 12, v[208:209]
	v_pk_mul_f32 v[226:227], v[168:169], v[210:211] op_sel_hi:[1,0]
	v_pk_mul_f32 v[228:229], v[166:167], v[210:211] op_sel_hi:[1,0]
	v_cvt_pk_bf16_f32 v208, v226, v227
	v_cvt_pk_bf16_f32 v209, v212, v213
	v_lshl_add_u64 v[212:213], s[26:27], 0, v[240:241]
	v_pk_mul_f32 v[230:231], v[164:165], v[210:211] op_sel_hi:[1,0]
	v_pk_mul_f32 v[232:233], v[130:131], v[210:211] op_sel_hi:[1,0]
	v_pk_mul_f32 v[234:235], v[128:129], v[210:211] op_sel_hi:[1,0]
	v_pk_mul_f32 v[236:237], v[122:123], v[210:211] op_sel_hi:[1,0]
	v_pk_mul_f32 v[238:239], v[120:121], v[210:211] op_sel_hi:[1,0]
	v_cvt_pk_bf16_f32 v210, v230, v231
	v_cvt_pk_bf16_f32 v211, v228, v229
	v_lshl_add_u64 v[212:213], v[212:213], 0, v[2:3]
	global_store_dwordx4 v[212:213], v[208:211], off
	s_nop 1
	v_cvt_pk_bf16_f32 v208, v234, v235
	v_cvt_pk_bf16_f32 v209, v232, v233
	v_cvt_pk_bf16_f32 v210, v238, v239
	v_cvt_pk_bf16_f32 v211, v236, v237
	global_store_dwordx4 v[212:213], v[208:211], off offset:256
.LBB0_1330:
	s_or_b64 exec, exec, s[10:11]
	v_or_b32_e32 v3, 32, v203
	v_cmp_lt_i32_e32 vcc, v3, v201
	s_and_saveexec_b64 s[10:11], vcc
	s_cbranch_execz .LBB0_1332
	v_mov_b32_e32 v208, v118
	v_mov_b32_e32 v210, v134
	v_mov_b32_e32 v3, v1
	v_ashrrev_i32_e32 v209, 31, v208
	v_pk_mul_f32 v[212:213], v[162:163], v[210:211] op_sel_hi:[1,0]
	v_lshlrev_b64 v[240:241], 12, v[208:209]
	v_pk_mul_f32 v[226:227], v[160:161], v[210:211] op_sel_hi:[1,0]
	v_pk_mul_f32 v[228:229], v[158:159], v[210:211] op_sel_hi:[1,0]
	v_cvt_pk_bf16_f32 v208, v226, v227
	v_cvt_pk_bf16_f32 v209, v212, v213
	v_lshl_add_u64 v[212:213], s[26:27], 0, v[240:241]
	v_pk_mul_f32 v[230:231], v[156:157], v[210:211] op_sel_hi:[1,0]
	v_pk_mul_f32 v[232:233], v[114:115], v[210:211] op_sel_hi:[1,0]
	v_pk_mul_f32 v[234:235], v[112:113], v[210:211] op_sel_hi:[1,0]
	v_pk_mul_f32 v[236:237], v[110:111], v[210:211] op_sel_hi:[1,0]
	v_pk_mul_f32 v[238:239], v[108:109], v[210:211] op_sel_hi:[1,0]
	v_cvt_pk_bf16_f32 v210, v230, v231
	v_cvt_pk_bf16_f32 v211, v228, v229
	v_lshl_add_u64 v[212:213], v[212:213], 0, v[2:3]
	global_store_dwordx4 v[212:213], v[208:211], off
	s_nop 1
	v_cvt_pk_bf16_f32 v208, v234, v235
	v_cvt_pk_bf16_f32 v209, v232, v233
	v_cvt_pk_bf16_f32 v210, v238, v239
	v_cvt_pk_bf16_f32 v211, v236, v237
	global_store_dwordx4 v[212:213], v[208:211], off offset:256
.LBB0_1332:
	s_or_b64 exec, exec, s[10:11]
	v_or_b32_e32 v3, 48, v203
	v_cmp_lt_i32_e32 vcc, v3, v201
	s_and_saveexec_b64 s[10:11], vcc
	s_cbranch_execz .LBB0_1334
	v_mov_b32_e32 v208, v119
	v_mov_b32_e32 v210, v135
	v_mov_b32_e32 v3, v1
	v_ashrrev_i32_e32 v209, 31, v208
	v_pk_mul_f32 v[212:213], v[154:155], v[210:211] op_sel_hi:[1,0]
	v_lshlrev_b64 v[240:241], 12, v[208:209]
	v_pk_mul_f32 v[226:227], v[152:153], v[210:211] op_sel_hi:[1,0]
	v_pk_mul_f32 v[228:229], v[150:151], v[210:211] op_sel_hi:[1,0]
	v_cvt_pk_bf16_f32 v208, v226, v227
	v_cvt_pk_bf16_f32 v209, v212, v213
	v_lshl_add_u64 v[212:213], s[26:27], 0, v[240:241]
	v_pk_mul_f32 v[230:231], v[148:149], v[210:211] op_sel_hi:[1,0]
	v_pk_mul_f32 v[232:233], v[106:107], v[210:211] op_sel_hi:[1,0]
	v_pk_mul_f32 v[234:235], v[104:105], v[210:211] op_sel_hi:[1,0]
	v_pk_mul_f32 v[236:237], v[102:103], v[210:211] op_sel_hi:[1,0]
	v_pk_mul_f32 v[238:239], v[100:101], v[210:211] op_sel_hi:[1,0]
	v_cvt_pk_bf16_f32 v210, v230, v231
	v_cvt_pk_bf16_f32 v211, v228, v229
	v_lshl_add_u64 v[212:213], v[212:213], 0, v[2:3]
	global_store_dwordx4 v[212:213], v[208:211], off
	s_nop 1
	v_cvt_pk_bf16_f32 v208, v234, v235
	v_cvt_pk_bf16_f32 v209, v232, v233
	v_cvt_pk_bf16_f32 v210, v238, v239
	v_cvt_pk_bf16_f32 v211, v236, v237
	global_store_dwordx4 v[212:213], v[208:211], off offset:256
; __device__ __forceinline__ unsigned cvt_pk_bf16(float lo, float hi) { unsigned r; asm volatile("v_cvt_pk_bf16_f32 %0, %1, %2" : "=v"(r) : "v"(lo), "v"(hi)); return r; }
;     template <class Tp> __device__ __forceinline__ Tp* w(size_t off) const { return (Tp*)(ws + off); }
;     __device__ __forceinline__ void operator()(const f32x4 (&acc)[2][2][4][2], const Unit& u, int wr, int wc, int fr, int fq) const {
;     ...
;             for (int m = 0; m < 4; ++m) { const int p = row0 + ai * HALF + m * 16;
;                 if (p < lim) { const float w = wrow[lb + p]; bf16_t* rowp = Y2 + (size_t)tsi[lb + p] * 2048 + col0;
; #pragma unroll
;                     for (int bj = 0; bj < 2; ++bj) { const f32x4 v0 = acc[ai][bj][m][0] * w, v1 = acc[ai][bj][m][1] * w;
;                         u32x4 o; o.x = cvt_pk_bf16(v0[0], v0[1]); o.y = cvt_pk_bf16(v0[2], v0[3]); o.z = cvt_pk_bf16(v1[0], v1[1]); o.w = cvt_pk_bf16(v1[2], v1[3]);
;                         *(u32x4*)(rowp + bj * HALF) = o; } } }
.LBB0_1334:
	s_or_b64 exec, exec, s[10:11]
	v_add_u32_e32 v3, 0x80, v203
	v_cmp_lt_i32_e32 vcc, v3, v201
	s_and_saveexec_b64 s[10:11], vcc
	s_cbranch_execz .LBB0_1336
	v_mov_b32_e32 v208, v124
	v_mov_b32_e32 v210, v140
	v_mov_b32_e32 v3, v1
	v_ashrrev_i32_e32 v209, 31, v208
	v_pk_mul_f32 v[212:213], v[98:99], v[210:211] op_sel_hi:[1,0]
	v_lshlrev_b64 v[240:241], 12, v[208:209]
	v_pk_mul_f32 v[226:227], v[96:97], v[210:211] op_sel_hi:[1,0]
	v_pk_mul_f32 v[228:229], v[94:95], v[210:211] op_sel_hi:[1,0]
	v_cvt_pk_bf16_f32 v208, v226, v227
	v_cvt_pk_bf16_f32 v209, v212, v213
	v_lshl_add_u64 v[212:213], s[26:27], 0, v[240:241]
	v_pk_mul_f32 v[230:231], v[92:93], v[210:211] op_sel_hi:[1,0]
	v_pk_mul_f32 v[232:233], v[66:67], v[210:211] op_sel_hi:[1,0]
	v_pk_mul_f32 v[234:235], v[64:65], v[210:211] op_sel_hi:[1,0]
	v_pk_mul_f32 v[236:237], v[62:63], v[210:211] op_sel_hi:[1,0]
	v_pk_mul_f32 v[238:239], v[60:61], v[210:211] op_sel_hi:[1,0]
	v_cvt_pk_bf16_f32 v210, v230, v231
	v_cvt_pk_bf16_f32 v211, v228, v229
	v_lshl_add_u64 v[212:213], v[212:213], 0, v[2:3]
	global_store_dwordx4 v[212:213], v[208:211], off
	s_nop 1
	v_cvt_pk_bf16_f32 v208, v234, v235
	v_cvt_pk_bf16_f32 v209, v232, v233
	v_cvt_pk_bf16_f32 v210, v238, v239
	v_cvt_pk_bf16_f32 v211, v236, v237
	global_store_dwordx4 v[212:213], v[208:211], off offset:256
.LBB0_1336:
	s_or_b64 exec, exec, s[10:11]
	v_add_u32_e32 v3, 0x90, v203
	v_cmp_lt_i32_e32 vcc, v3, v201
	s_and_saveexec_b64 s[10:11], vcc
	s_cbranch_execz .LBB0_1338
	v_mov_b32_e32 v208, v125
	v_mov_b32_e32 v210, v141
	v_mov_b32_e32 v3, v1
	v_ashrrev_i32_e32 v209, 31, v208
	v_pk_mul_f32 v[212:213], v[90:91], v[210:211] op_sel_hi:[1,0]
	v_lshlrev_b64 v[240:241], 12, v[208:209]
	v_pk_mul_f32 v[226:227], v[88:89], v[210:211] op_sel_hi:[1,0]
	v_pk_mul_f32 v[228:229], v[86:87], v[210:211] op_sel_hi:[1,0]
	v_cvt_pk_bf16_f32 v208, v226, v227
	v_cvt_pk_bf16_f32 v209, v212, v213
	v_lshl_add_u64 v[212:213], s[26:27], 0, v[240:241]
	v_pk_mul_f32 v[230:231], v[84:85], v[210:211] op_sel_hi:[1,0]
	v_pk_mul_f32 v[232:233], v[54:55], v[210:211] op_sel_hi:[1,0]
	v_pk_mul_f32 v[234:235], v[52:53], v[210:211] op_sel_hi:[1,0]
	v_pk_mul_f32 v[236:237], v[50:51], v[210:211] op_sel_hi:[1,0]
	v_pk_mul_f32 v[238:239], v[48:49], v[210:211] op_sel_hi:[1,0]
	v_cvt_pk_bf16_f32 v210, v230, v231
	v_cvt_pk_bf16_f32 v211, v228, v229
	v_lshl_add_u64 v[212:213], v[212:213], 0, v[2:3]
	global_store_dwordx4 v[212:213], v[208:211], off
	s_nop 1
	v_cvt_pk_bf16_f32 v208, v234, v235
	v_cvt_pk_bf16_f32 v209, v232, v233
	v_cvt_pk_bf16_f32 v210, v238, v239
	v_cvt_pk_bf16_f32 v211, v236, v237
	global_store_dwordx4 v[212:213], v[208:211], off offset:256
.LBB0_1338:
	s_or_b64 exec, exec, s[10:11]
	v_add_u32_e32 v3, 0xa0, v203
	v_cmp_lt_i32_e32 vcc, v3, v201
	s_and_saveexec_b64 s[10:11], vcc
	s_cbranch_execz .LBB0_1340
	v_mov_b32_e32 v208, v126
	v_mov_b32_e32 v210, v142
	v_mov_b32_e32 v3, v1
	v_ashrrev_i32_e32 v209, 31, v208
	v_pk_mul_f32 v[212:213], v[82:83], v[210:211] op_sel_hi:[1,0]
	v_lshlrev_b64 v[240:241], 12, v[208:209]
	v_pk_mul_f32 v[226:227], v[80:81], v[210:211] op_sel_hi:[1,0]
	v_pk_mul_f32 v[228:229], v[78:79], v[210:211] op_sel_hi:[1,0]
	v_cvt_pk_bf16_f32 v208, v226, v227
	v_cvt_pk_bf16_f32 v209, v212, v213
	v_lshl_add_u64 v[212:213], s[26:27], 0, v[240:241]
	v_pk_mul_f32 v[230:231], v[76:77], v[210:211] op_sel_hi:[1,0]
	v_pk_mul_f32 v[232:233], v[46:47], v[210:211] op_sel_hi:[1,0]
	v_pk_mul_f32 v[234:235], v[44:45], v[210:211] op_sel_hi:[1,0]
	v_pk_mul_f32 v[236:237], v[42:43], v[210:211] op_sel_hi:[1,0]
	v_pk_mul_f32 v[238:239], v[40:41], v[210:211] op_sel_hi:[1,0]
	v_cvt_pk_bf16_f32 v210, v230, v231
	v_cvt_pk_bf16_f32 v211, v228, v229
	v_lshl_add_u64 v[212:213], v[212:213], 0, v[2:3]
	global_store_dwordx4 v[212:213], v[208:211], off
	s_nop 1
	v_cvt_pk_bf16_f32 v208, v234, v235
	v_cvt_pk_bf16_f32 v209, v232, v233
	v_cvt_pk_bf16_f32 v210, v238, v239
	v_cvt_pk_bf16_f32 v211, v236, v237
	global_store_dwordx4 v[212:213], v[208:211], off offset:256
.LBB0_1340:
	s_or_b64 exec, exec, s[10:11]
	v_add_u32_e32 v3, 0xb0, v203
	v_cmp_lt_i32_e32 vcc, v3, v201
	s_and_saveexec_b64 s[10:11], vcc
	s_cbranch_execz .LBB0_1342
	v_mov_b32_e32 v208, v127
	v_mov_b32_e32 v210, v143
	v_mov_b32_e32 v3, v1
	v_ashrrev_i32_e32 v209, 31, v208
	v_pk_mul_f32 v[212:213], v[74:75], v[210:211] op_sel_hi:[1,0]
	v_lshlrev_b64 v[240:241], 12, v[208:209]
	v_pk_mul_f32 v[226:227], v[72:73], v[210:211] op_sel_hi:[1,0]
	v_pk_mul_f32 v[228:229], v[70:71], v[210:211] op_sel_hi:[1,0]
	v_cvt_pk_bf16_f32 v208, v226, v227
	v_cvt_pk_bf16_f32 v209, v212, v213
	v_lshl_add_u64 v[212:213], s[26:27], 0, v[240:241]
	v_pk_mul_f32 v[230:231], v[68:69], v[210:211] op_sel_hi:[1,0]
	v_pk_mul_f32 v[232:233], v[38:39], v[210:211] op_sel_hi:[1,0]
	v_pk_mul_f32 v[234:235], v[36:37], v[210:211] op_sel_hi:[1,0]
	v_pk_mul_f32 v[236:237], v[34:35], v[210:211] op_sel_hi:[1,0]
	v_pk_mul_f32 v[238:239], v[32:33], v[210:211] op_sel_hi:[1,0]
	v_cvt_pk_bf16_f32 v210, v230, v231
	v_cvt_pk_bf16_f32 v211, v228, v229
	v_lshl_add_u64 v[2:3], v[212:213], 0, v[2:3]
	global_store_dwordx4 v[2:3], v[208:211], off
	s_nop 1
	v_cvt_pk_bf16_f32 v208, v234, v235
	v_cvt_pk_bf16_f32 v209, v232, v233
	v_cvt_pk_bf16_f32 v210, v238, v239
	v_cvt_pk_bf16_f32 v211, v236, v237
	global_store_dwordx4 v[2:3], v[208:211], off offset:256
